# t17
# baseline (speedup 1.0000x reference)
_Z11align_fusedPKfS0_PKiPf:
	s_load_dwordx8 s[4:11], s[0:1], 0x0
	s_sub_u32 s2, 0x1fff, s2
	s_mul_i32 s12, s2, 0x5dc0
	v_and_b32_e32 v7, 63, v0
	v_readfirstlane_b32 s13, v0
	v_lshlrev_b32_e32 v1, 4, v7
	v_mul_u32_u24_e32 v3, 12, v7
	s_mul_i32 s18, s13, 96
	s_mul_i32 s19, s13, 48
	s_mul_i32 s3, s13, 6
	s_sub_u32 s3, 0x49c, s3
	v_cmp_gt_u32_e64 s[14:15], s3, v7
	v_add_u32_e32 v2, s19, v1
	v_add_u32_e32 v3, s19, v3
	v_add_u32_e32 v4, 0x600, v3
	s_add_u32 s12, s12, s18
	s_add_u32 s12, s12, 0x800
	s_waitcnt lgkmcnt(0)
	s_add_u32 s4, s4, s12
	s_addc_u32 s5, s5, 0
	s_add_u32 s10, s10, s12
	s_addc_u32 s11, s11, 0
	s_cmp_lg_u32 s13, 0
	s_cbranch_scc1 .Lbulk_waves
	global_load_dwordx3 v[44:46], v3, s[6:7] nt
	s_load_dwordx16 s[16:31], s[8:9], 0x0
	s_load_dwordx16 s[32:47], s[8:9], 0x40
	s_load_dwordx16 s[48:63], s[8:9], 0x80
	s_waitcnt lgkmcnt(0)
	v_writelane_b32 v5, s16, 0
	v_writelane_b32 v5, s17, 1
	v_writelane_b32 v5, s18, 2
	v_writelane_b32 v5, s19, 3
	v_writelane_b32 v5, s20, 4
	v_writelane_b32 v5, s21, 5
	v_writelane_b32 v5, s22, 6
	v_writelane_b32 v5, s23, 7
	v_writelane_b32 v5, s24, 8
	v_writelane_b32 v5, s25, 9
	v_writelane_b32 v5, s26, 10
	v_writelane_b32 v5, s27, 11
	v_writelane_b32 v5, s28, 12
	v_writelane_b32 v5, s29, 13
	v_writelane_b32 v5, s30, 14
	v_writelane_b32 v5, s31, 15
	s_load_dwordx16 s[16:31], s[8:9], 0xc0
	v_writelane_b32 v5, s32, 16
	v_writelane_b32 v5, s33, 17
	v_writelane_b32 v5, s34, 18
	v_writelane_b32 v5, s35, 19
	v_writelane_b32 v5, s36, 20
	v_writelane_b32 v5, s37, 21
	v_writelane_b32 v5, s38, 22
	v_writelane_b32 v5, s39, 23
	v_writelane_b32 v5, s40, 24
	v_writelane_b32 v5, s41, 25
	v_writelane_b32 v5, s42, 26
	v_writelane_b32 v5, s43, 27
	v_writelane_b32 v5, s44, 28
	v_writelane_b32 v5, s45, 29
	v_writelane_b32 v5, s46, 30
	v_writelane_b32 v5, s47, 31
	v_writelane_b32 v5, s48, 32
	v_writelane_b32 v5, s49, 33
	v_writelane_b32 v5, s50, 34
	v_writelane_b32 v5, s51, 35
	v_writelane_b32 v5, s52, 36
	v_writelane_b32 v5, s53, 37
	v_writelane_b32 v5, s54, 38
	v_writelane_b32 v5, s55, 39
	v_writelane_b32 v5, s56, 40
	v_writelane_b32 v5, s57, 41
	v_writelane_b32 v5, s58, 42
	v_writelane_b32 v5, s59, 43
	v_writelane_b32 v5, s60, 44
	v_writelane_b32 v5, s61, 45
	v_writelane_b32 v5, s62, 46
	v_writelane_b32 v5, s63, 47
	s_waitcnt lgkmcnt(0)
	v_writelane_b32 v5, s16, 48
	v_writelane_b32 v5, s17, 49
	v_writelane_b32 v5, s18, 50
	v_writelane_b32 v5, s19, 51
	v_writelane_b32 v5, s20, 52
	v_writelane_b32 v5, s21, 53
	v_writelane_b32 v5, s22, 54
	v_writelane_b32 v5, s23, 55
	v_writelane_b32 v5, s24, 56
	v_writelane_b32 v5, s25, 57
	v_writelane_b32 v5, s26, 58
	v_writelane_b32 v5, s27, 59
	v_writelane_b32 v5, s28, 60
	v_writelane_b32 v5, s29, 61
	v_writelane_b32 v5, s30, 62
	v_writelane_b32 v5, s31, 63
	v_mul_u32_u24_e32 v5, 12, v5
	global_load_dwordx3 v[48:50], v5, s[4:5] offset:-2048 nt
	global_load_dwordx4 v[8:11], v1, s[4:5] offset:-2048 nt
	global_load_dwordx4 v[12:15], v1, s[4:5] offset:-1024 nt
	global_load_dwordx4 v[16:19], v1, s[4:5] offset:0 nt
	global_load_dwordx4 v[20:23], v1, s[4:5] offset:1024 nt
	global_load_dwordx4 v[24:27], v1, s[4:5] offset:2048 nt
	global_load_dwordx4 v[28:31], v1, s[4:5] offset:3072 nt
	s_mov_b32 s20, 0
	s_mov_b32 s21, 0x10000
	s_mov_b32 s22, 0
	s_mov_b32 s23, 0x20000
	s_mov_b32 s24, 0
	s_mov_b32 s25, 0x40000
	s_mov_b32 s26, 0
	s_mov_b32 s27, 0x80000
	s_waitcnt vmcnt(7)
	v_add_f32_dpp v52, v44, v44 quad_perm:[1,0,3,2] row_mask:0xf bank_mask:0xf
	v_add_f32_dpp v53, v45, v45 quad_perm:[1,0,3,2] row_mask:0xf bank_mask:0xf
	v_add_f32_dpp v54, v46, v46 quad_perm:[1,0,3,2] row_mask:0xf bank_mask:0xf
	v_add_f32_dpp v52, v52, v52 quad_perm:[2,3,0,1] row_mask:0xf bank_mask:0xf
	v_add_f32_dpp v53, v53, v53 quad_perm:[2,3,0,1] row_mask:0xf bank_mask:0xf
	v_add_f32_dpp v54, v54, v54 quad_perm:[2,3,0,1] row_mask:0xf bank_mask:0xf
	v_add_f32_dpp v52, v52, v52 row_half_mirror row_mask:0xf bank_mask:0xf
	v_add_f32_dpp v53, v53, v53 row_half_mirror row_mask:0xf bank_mask:0xf
	v_add_f32_dpp v54, v54, v54 row_half_mirror row_mask:0xf bank_mask:0xf
	v_add_f32_dpp v52, v52, v52 row_mirror row_mask:0xf bank_mask:0xf
	v_add_f32_dpp v53, v53, v53 row_mirror row_mask:0xf bank_mask:0xf
	v_add_f32_dpp v54, v54, v54 row_mirror row_mask:0xf bank_mask:0xf
	v_add_f32_dpp v52, v52, v52 row_bcast:15 row_mask:0xa bank_mask:0xf
	v_add_f32_dpp v53, v53, v53 row_bcast:15 row_mask:0xa bank_mask:0xf
	v_add_f32_dpp v54, v54, v54 row_bcast:15 row_mask:0xa bank_mask:0xf
	v_add_f32_dpp v52, v52, v52 row_bcast:31 row_mask:0xc bank_mask:0xf
	v_add_f32_dpp v53, v53, v53 row_bcast:31 row_mask:0xc bank_mask:0xf
	v_add_f32_dpp v54, v54, v54 row_bcast:31 row_mask:0xc bank_mask:0xf
	v_readlane_b32 s28, v52, 63
	v_readlane_b32 s29, v53, 63
	v_readlane_b32 s30, v54, 63
	v_mov_b32_e32 v52, s28
	v_mov_b32_e32 v53, s29
	v_mov_b32_e32 v54, s30
	v_fmac_f32_e32 v44, 0xbc800000, v52
	v_fmac_f32_e32 v45, 0xbc800000, v53
	v_fmac_f32_e32 v46, 0xbc800000, v54
	s_waitcnt vmcnt(6)
	v_add_f32_dpp v52, v48, v48 quad_perm:[1,0,3,2] row_mask:0xf bank_mask:0xf
	v_add_f32_dpp v53, v49, v49 quad_perm:[1,0,3,2] row_mask:0xf bank_mask:0xf
	v_add_f32_dpp v54, v50, v50 quad_perm:[1,0,3,2] row_mask:0xf bank_mask:0xf
	v_add_f32_dpp v52, v52, v52 quad_perm:[2,3,0,1] row_mask:0xf bank_mask:0xf
	v_add_f32_dpp v53, v53, v53 quad_perm:[2,3,0,1] row_mask:0xf bank_mask:0xf
	v_add_f32_dpp v54, v54, v54 quad_perm:[2,3,0,1] row_mask:0xf bank_mask:0xf
	v_add_f32_dpp v52, v52, v52 row_half_mirror row_mask:0xf bank_mask:0xf
	v_add_f32_dpp v53, v53, v53 row_half_mirror row_mask:0xf bank_mask:0xf
	v_add_f32_dpp v54, v54, v54 row_half_mirror row_mask:0xf bank_mask:0xf
	v_add_f32_dpp v52, v52, v52 row_mirror row_mask:0xf bank_mask:0xf
	v_add_f32_dpp v53, v53, v53 row_mirror row_mask:0xf bank_mask:0xf
	v_add_f32_dpp v54, v54, v54 row_mirror row_mask:0xf bank_mask:0xf
	v_add_f32_dpp v52, v52, v52 row_bcast:15 row_mask:0xa bank_mask:0xf
	v_add_f32_dpp v53, v53, v53 row_bcast:15 row_mask:0xa bank_mask:0xf
	v_add_f32_dpp v54, v54, v54 row_bcast:15 row_mask:0xa bank_mask:0xf
	v_add_f32_dpp v52, v52, v52 row_bcast:31 row_mask:0xc bank_mask:0xf
	v_add_f32_dpp v53, v53, v53 row_bcast:31 row_mask:0xc bank_mask:0xf
	v_add_f32_dpp v54, v54, v54 row_bcast:31 row_mask:0xc bank_mask:0xf
	v_readlane_b32 s32, v52, 63
	v_readlane_b32 s33, v53, 63
	v_readlane_b32 s34, v54, 63
	v_mov_b32_e32 v52, s32
	v_mov_b32_e32 v53, s33
	v_mov_b32_e32 v54, s34
	v_fmac_f32_e32 v48, 0xbc800000, v52
	v_fmac_f32_e32 v49, 0xbc800000, v53
	v_fmac_f32_e32 v50, 0xbc800000, v54
	v_mul_f32_e32 v52, v48, v44
	v_mul_f32_e32 v53, v48, v45
	v_mul_f32_e32 v54, v48, v46
	v_mul_f32_e32 v55, v49, v44
	v_mul_f32_e32 v56, v49, v45
	v_mul_f32_e32 v57, v49, v46
	v_mul_f32_e32 v58, v50, v44
	v_mul_f32_e32 v59, v50, v45
	v_mul_f32_e32 v60, v50, v46
	v_add_f32_dpp v52, v52, v52 quad_perm:[1,0,3,2] row_mask:0xf bank_mask:0xf
	v_add_f32_dpp v53, v53, v53 quad_perm:[1,0,3,2] row_mask:0xf bank_mask:0xf
	v_add_f32_dpp v54, v54, v54 quad_perm:[1,0,3,2] row_mask:0xf bank_mask:0xf
	v_add_f32_dpp v55, v55, v55 quad_perm:[1,0,3,2] row_mask:0xf bank_mask:0xf
	v_add_f32_dpp v56, v56, v56 quad_perm:[1,0,3,2] row_mask:0xf bank_mask:0xf
	v_add_f32_dpp v57, v57, v57 quad_perm:[1,0,3,2] row_mask:0xf bank_mask:0xf
	v_add_f32_dpp v58, v58, v58 quad_perm:[1,0,3,2] row_mask:0xf bank_mask:0xf
	v_add_f32_dpp v59, v59, v59 quad_perm:[1,0,3,2] row_mask:0xf bank_mask:0xf
	v_add_f32_dpp v60, v60, v60 quad_perm:[1,0,3,2] row_mask:0xf bank_mask:0xf
	v_add_f32_dpp v52, v52, v52 quad_perm:[2,3,0,1] row_mask:0xf bank_mask:0xf
	v_add_f32_dpp v53, v53, v53 quad_perm:[2,3,0,1] row_mask:0xf bank_mask:0xf
	v_add_f32_dpp v54, v54, v54 quad_perm:[2,3,0,1] row_mask:0xf bank_mask:0xf
	v_add_f32_dpp v55, v55, v55 quad_perm:[2,3,0,1] row_mask:0xf bank_mask:0xf
	v_add_f32_dpp v56, v56, v56 quad_perm:[2,3,0,1] row_mask:0xf bank_mask:0xf
	v_add_f32_dpp v57, v57, v57 quad_perm:[2,3,0,1] row_mask:0xf bank_mask:0xf
	v_add_f32_dpp v58, v58, v58 quad_perm:[2,3,0,1] row_mask:0xf bank_mask:0xf
	v_add_f32_dpp v59, v59, v59 quad_perm:[2,3,0,1] row_mask:0xf bank_mask:0xf
	v_add_f32_dpp v60, v60, v60 quad_perm:[2,3,0,1] row_mask:0xf bank_mask:0xf
	v_add_f32_dpp v52, v52, v52 row_half_mirror row_mask:0xf bank_mask:0xf
	v_add_f32_dpp v53, v53, v53 row_half_mirror row_mask:0xf bank_mask:0xf
	v_add_f32_dpp v54, v54, v54 row_half_mirror row_mask:0xf bank_mask:0xf
	v_add_f32_dpp v55, v55, v55 row_half_mirror row_mask:0xf bank_mask:0xf
	v_add_f32_dpp v56, v56, v56 row_half_mirror row_mask:0xf bank_mask:0xf
	v_add_f32_dpp v57, v57, v57 row_half_mirror row_mask:0xf bank_mask:0xf
	v_add_f32_dpp v58, v58, v58 row_half_mirror row_mask:0xf bank_mask:0xf
	v_add_f32_dpp v59, v59, v59 row_half_mirror row_mask:0xf bank_mask:0xf
	v_add_f32_dpp v60, v60, v60 row_half_mirror row_mask:0xf bank_mask:0xf
	v_add_f32_dpp v52, v52, v52 row_mirror row_mask:0xf bank_mask:0xf
	v_add_f32_dpp v53, v53, v53 row_mirror row_mask:0xf bank_mask:0xf
	v_add_f32_dpp v54, v54, v54 row_mirror row_mask:0xf bank_mask:0xf
	v_add_f32_dpp v55, v55, v55 row_mirror row_mask:0xf bank_mask:0xf
	v_add_f32_dpp v56, v56, v56 row_mirror row_mask:0xf bank_mask:0xf
	v_add_f32_dpp v57, v57, v57 row_mirror row_mask:0xf bank_mask:0xf
	v_add_f32_dpp v58, v58, v58 row_mirror row_mask:0xf bank_mask:0xf
	v_add_f32_dpp v59, v59, v59 row_mirror row_mask:0xf bank_mask:0xf
	v_add_f32_dpp v60, v60, v60 row_mirror row_mask:0xf bank_mask:0xf
	v_add_f32_dpp v52, v52, v52 row_bcast:15 row_mask:0xa bank_mask:0xf
	v_add_f32_dpp v53, v53, v53 row_bcast:15 row_mask:0xa bank_mask:0xf
	v_add_f32_dpp v54, v54, v54 row_bcast:15 row_mask:0xa bank_mask:0xf
	v_add_f32_dpp v55, v55, v55 row_bcast:15 row_mask:0xa bank_mask:0xf
	v_add_f32_dpp v56, v56, v56 row_bcast:15 row_mask:0xa bank_mask:0xf
	v_add_f32_dpp v57, v57, v57 row_bcast:15 row_mask:0xa bank_mask:0xf
	v_add_f32_dpp v58, v58, v58 row_bcast:15 row_mask:0xa bank_mask:0xf
	v_add_f32_dpp v59, v59, v59 row_bcast:15 row_mask:0xa bank_mask:0xf
	v_add_f32_dpp v60, v60, v60 row_bcast:15 row_mask:0xa bank_mask:0xf
	v_add_f32_dpp v52, v52, v52 row_bcast:31 row_mask:0xc bank_mask:0xf
	v_add_f32_dpp v53, v53, v53 row_bcast:31 row_mask:0xc bank_mask:0xf
	v_add_f32_dpp v54, v54, v54 row_bcast:31 row_mask:0xc bank_mask:0xf
	v_add_f32_dpp v55, v55, v55 row_bcast:31 row_mask:0xc bank_mask:0xf
	v_add_f32_dpp v56, v56, v56 row_bcast:31 row_mask:0xc bank_mask:0xf
	v_add_f32_dpp v57, v57, v57 row_bcast:31 row_mask:0xc bank_mask:0xf
	v_add_f32_dpp v58, v58, v58 row_bcast:31 row_mask:0xc bank_mask:0xf
	v_add_f32_dpp v59, v59, v59 row_bcast:31 row_mask:0xc bank_mask:0xf
	v_add_f32_dpp v60, v60, v60 row_bcast:31 row_mask:0xc bank_mask:0xf
	v_cndmask_b32_e64 v52, v52, v55, s[22:23]
	v_cndmask_b32_e64 v53, v53, v56, s[22:23]
	v_cndmask_b32_e64 v54, v54, v57, s[22:23]
	v_cndmask_b32_e64 v52, v52, v58, s[24:25]
	v_cndmask_b32_e64 v53, v53, v59, s[24:25]
	v_cndmask_b32_e64 v54, v54, v60, s[24:25]
	v_cndmask_b32_e64 v52, v52, 0, s[26:27]
	v_cndmask_b32_e64 v53, v53, 0, s[26:27]
	v_cndmask_b32_e64 v54, v54, 0, s[26:27]
	v_cndmask_b32_e64 v40, 0, 1.0, s[20:21]
	v_cndmask_b32_e64 v41, 0, 1.0, s[22:23]
	v_cndmask_b32_e64 v42, 0, 1.0, s[24:25]
	v_mul_f32_e32 v55, v52, v52
	v_mul_f32_e32 v56, v53, v53
	v_mul_f32_e32 v57, v52, v53
	v_add_f32_dpp v55, v55, v55 quad_perm:[1,0,3,2] row_mask:0xf bank_mask:0xf
	v_add_f32_dpp v56, v56, v56 quad_perm:[1,0,3,2] row_mask:0xf bank_mask:0xf
	v_add_f32_dpp v57, v57, v57 quad_perm:[1,0,3,2] row_mask:0xf bank_mask:0xf
	v_add_f32_dpp v55, v55, v55 quad_perm:[2,3,0,1] row_mask:0xf bank_mask:0xf
	v_add_f32_dpp v56, v56, v56 quad_perm:[2,3,0,1] row_mask:0xf bank_mask:0xf
	v_add_f32_dpp v57, v57, v57 quad_perm:[2,3,0,1] row_mask:0xf bank_mask:0xf
	v_sub_f32_e32 v60, v56, v55
	v_mul_f32_e32 v58, v57, v57
	v_cmp_gt_f32_e32 vcc, 0, v60
	v_mul_f32_e32 v59, v60, v60
	v_fmac_f32_e32 v59, 4.0, v58
	v_sqrt_f32_e32 v59, v59
	s_nop 0
	v_add_f32_e64 v59, |v60|, v59
	v_add_f32_e32 v59, 0x0da24260, v59
	v_rcp_f32_e32 v59, v59
	v_add_f32_e32 v58, v57, v57
	v_mul_f32_e32 v59, v58, v59
	v_cndmask_b32_e64 v59, v59, -v59, vcc
	v_fma_f32 v58, v59, v59, 1.0
	v_rsq_f32_e32 v61, v58
	s_nop 0
	v_mul_f32_e32 v62, v61, v59
	v_mul_f32_e32 v55, v62, v53
	v_mul_f32_e32 v56, v62, v52
	v_fma_f32 v52, v61, v52, -v55
	v_fma_f32 v53, v61, v53, v56
	v_mul_f32_e32 v55, v52, v52
	v_mul_f32_e32 v56, v54, v54
	v_mul_f32_e32 v57, v52, v54
	v_add_f32_dpp v55, v55, v55 quad_perm:[1,0,3,2] row_mask:0xf bank_mask:0xf
	v_add_f32_dpp v56, v56, v56 quad_perm:[1,0,3,2] row_mask:0xf bank_mask:0xf
	v_add_f32_dpp v57, v57, v57 quad_perm:[1,0,3,2] row_mask:0xf bank_mask:0xf
	v_add_f32_dpp v55, v55, v55 quad_perm:[2,3,0,1] row_mask:0xf bank_mask:0xf
	v_add_f32_dpp v56, v56, v56 quad_perm:[2,3,0,1] row_mask:0xf bank_mask:0xf
	v_add_f32_dpp v57, v57, v57 quad_perm:[2,3,0,1] row_mask:0xf bank_mask:0xf
	v_sub_f32_e32 v60, v56, v55
	v_mul_f32_e32 v58, v57, v57
	v_cmp_gt_f32_e32 vcc, 0, v60
	v_mul_f32_e32 v59, v60, v60
	v_fmac_f32_e32 v59, 4.0, v58
	v_sqrt_f32_e32 v59, v59
	v_mul_f32_e32 v63, v62, v41
	v_mul_f32_e32 v43, v62, v40
	v_fma_f32 v40, v61, v40, -v63
	v_fma_f32 v41, v61, v41, v43
	v_add_f32_e64 v59, |v60|, v59
	v_add_f32_e32 v59, 0x0da24260, v59
	v_rcp_f32_e32 v59, v59
	v_add_f32_e32 v58, v57, v57
	v_mul_f32_e32 v59, v58, v59
	v_cndmask_b32_e64 v59, v59, -v59, vcc
	v_fma_f32 v58, v59, v59, 1.0
	v_rsq_f32_e32 v61, v58
	s_nop 0
	v_mul_f32_e32 v62, v61, v59
	v_mul_f32_e32 v55, v62, v54
	v_mul_f32_e32 v56, v62, v52
	v_fma_f32 v52, v61, v52, -v55
	v_fma_f32 v54, v61, v54, v56
	v_mul_f32_e32 v55, v53, v53
	v_mul_f32_e32 v56, v54, v54
	v_mul_f32_e32 v57, v53, v54
	v_add_f32_dpp v55, v55, v55 quad_perm:[1,0,3,2] row_mask:0xf bank_mask:0xf
	v_add_f32_dpp v56, v56, v56 quad_perm:[1,0,3,2] row_mask:0xf bank_mask:0xf
	v_add_f32_dpp v57, v57, v57 quad_perm:[1,0,3,2] row_mask:0xf bank_mask:0xf
	v_add_f32_dpp v55, v55, v55 quad_perm:[2,3,0,1] row_mask:0xf bank_mask:0xf
	v_add_f32_dpp v56, v56, v56 quad_perm:[2,3,0,1] row_mask:0xf bank_mask:0xf
	v_add_f32_dpp v57, v57, v57 quad_perm:[2,3,0,1] row_mask:0xf bank_mask:0xf
	v_sub_f32_e32 v60, v56, v55
	v_mul_f32_e32 v58, v57, v57
	v_cmp_gt_f32_e32 vcc, 0, v60
	v_mul_f32_e32 v59, v60, v60
	v_fmac_f32_e32 v59, 4.0, v58
	v_sqrt_f32_e32 v59, v59
	v_mul_f32_e32 v63, v62, v42
	v_mul_f32_e32 v43, v62, v40
	v_fma_f32 v40, v61, v40, -v63
	v_fma_f32 v42, v61, v42, v43
	v_add_f32_e64 v59, |v60|, v59
	v_add_f32_e32 v59, 0x0da24260, v59
	v_rcp_f32_e32 v59, v59
	v_add_f32_e32 v58, v57, v57
	v_mul_f32_e32 v59, v58, v59
	v_cndmask_b32_e64 v59, v59, -v59, vcc
	v_fma_f32 v58, v59, v59, 1.0
	v_rsq_f32_e32 v61, v58
	s_nop 0
	v_mul_f32_e32 v62, v61, v59
	v_mul_f32_e32 v55, v62, v54
	v_mul_f32_e32 v56, v62, v53
	v_fma_f32 v53, v61, v53, -v55
	v_fma_f32 v54, v61, v54, v56
	v_mul_f32_e32 v55, v52, v52
	v_mul_f32_e32 v56, v53, v53
	v_mul_f32_e32 v57, v52, v53
	v_add_f32_dpp v55, v55, v55 quad_perm:[1,0,3,2] row_mask:0xf bank_mask:0xf
	v_add_f32_dpp v56, v56, v56 quad_perm:[1,0,3,2] row_mask:0xf bank_mask:0xf
	v_add_f32_dpp v57, v57, v57 quad_perm:[1,0,3,2] row_mask:0xf bank_mask:0xf
	v_add_f32_dpp v55, v55, v55 quad_perm:[2,3,0,1] row_mask:0xf bank_mask:0xf
	v_add_f32_dpp v56, v56, v56 quad_perm:[2,3,0,1] row_mask:0xf bank_mask:0xf
	v_add_f32_dpp v57, v57, v57 quad_perm:[2,3,0,1] row_mask:0xf bank_mask:0xf
	v_sub_f32_e32 v60, v56, v55
	v_mul_f32_e32 v58, v57, v57
	v_cmp_gt_f32_e32 vcc, 0, v60
	v_mul_f32_e32 v59, v60, v60
	v_fmac_f32_e32 v59, 4.0, v58
	v_sqrt_f32_e32 v59, v59
	v_mul_f32_e32 v63, v62, v42
	v_mul_f32_e32 v43, v62, v41
	v_fma_f32 v41, v61, v41, -v63
	v_fma_f32 v42, v61, v42, v43
	v_add_f32_e64 v59, |v60|, v59
	v_add_f32_e32 v59, 0x0da24260, v59
	v_rcp_f32_e32 v59, v59
	v_add_f32_e32 v58, v57, v57
	v_mul_f32_e32 v59, v58, v59
	v_cndmask_b32_e64 v59, v59, -v59, vcc
	v_fma_f32 v58, v59, v59, 1.0
	v_rsq_f32_e32 v61, v58
	s_nop 0
	v_mul_f32_e32 v62, v61, v59
	v_mul_f32_e32 v55, v62, v53
	v_mul_f32_e32 v56, v62, v52
	v_fma_f32 v52, v61, v52, -v55
	v_fma_f32 v53, v61, v53, v56
	v_mul_f32_e32 v55, v52, v52
	v_mul_f32_e32 v56, v54, v54
	v_mul_f32_e32 v57, v52, v54
	v_add_f32_dpp v55, v55, v55 quad_perm:[1,0,3,2] row_mask:0xf bank_mask:0xf
	v_add_f32_dpp v56, v56, v56 quad_perm:[1,0,3,2] row_mask:0xf bank_mask:0xf
	v_add_f32_dpp v57, v57, v57 quad_perm:[1,0,3,2] row_mask:0xf bank_mask:0xf
	v_add_f32_dpp v55, v55, v55 quad_perm:[2,3,0,1] row_mask:0xf bank_mask:0xf
	v_add_f32_dpp v56, v56, v56 quad_perm:[2,3,0,1] row_mask:0xf bank_mask:0xf
	v_add_f32_dpp v57, v57, v57 quad_perm:[2,3,0,1] row_mask:0xf bank_mask:0xf
	v_sub_f32_e32 v60, v56, v55
	v_mul_f32_e32 v58, v57, v57
	v_cmp_gt_f32_e32 vcc, 0, v60
	v_mul_f32_e32 v59, v60, v60
	v_fmac_f32_e32 v59, 4.0, v58
	v_sqrt_f32_e32 v59, v59
	v_mul_f32_e32 v63, v62, v41
	v_mul_f32_e32 v43, v62, v40
	v_fma_f32 v40, v61, v40, -v63
	v_fma_f32 v41, v61, v41, v43
	v_add_f32_e64 v59, |v60|, v59
	v_add_f32_e32 v59, 0x0da24260, v59
	v_rcp_f32_e32 v59, v59
	v_add_f32_e32 v58, v57, v57
	v_mul_f32_e32 v59, v58, v59
	v_cndmask_b32_e64 v59, v59, -v59, vcc
	v_fma_f32 v58, v59, v59, 1.0
	v_rsq_f32_e32 v61, v58
	s_nop 0
	v_mul_f32_e32 v62, v61, v59
	v_mul_f32_e32 v55, v62, v54
	v_mul_f32_e32 v56, v62, v52
	v_fma_f32 v52, v61, v52, -v55
	v_fma_f32 v54, v61, v54, v56
	v_mul_f32_e32 v55, v53, v53
	v_mul_f32_e32 v56, v54, v54
	v_mul_f32_e32 v57, v53, v54
	v_add_f32_dpp v55, v55, v55 quad_perm:[1,0,3,2] row_mask:0xf bank_mask:0xf
	v_add_f32_dpp v56, v56, v56 quad_perm:[1,0,3,2] row_mask:0xf bank_mask:0xf
	v_add_f32_dpp v57, v57, v57 quad_perm:[1,0,3,2] row_mask:0xf bank_mask:0xf
	v_add_f32_dpp v55, v55, v55 quad_perm:[2,3,0,1] row_mask:0xf bank_mask:0xf
	v_add_f32_dpp v56, v56, v56 quad_perm:[2,3,0,1] row_mask:0xf bank_mask:0xf
	v_add_f32_dpp v57, v57, v57 quad_perm:[2,3,0,1] row_mask:0xf bank_mask:0xf
	v_sub_f32_e32 v60, v56, v55
	v_mul_f32_e32 v58, v57, v57
	v_cmp_gt_f32_e32 vcc, 0, v60
	v_mul_f32_e32 v59, v60, v60
	v_fmac_f32_e32 v59, 4.0, v58
	v_sqrt_f32_e32 v59, v59
	v_mul_f32_e32 v63, v62, v42
	v_mul_f32_e32 v43, v62, v40
	v_fma_f32 v40, v61, v40, -v63
	v_fma_f32 v42, v61, v42, v43
	v_add_f32_e64 v59, |v60|, v59
	v_add_f32_e32 v59, 0x0da24260, v59
	v_rcp_f32_e32 v59, v59
	v_add_f32_e32 v58, v57, v57
	v_mul_f32_e32 v59, v58, v59
	v_cndmask_b32_e64 v59, v59, -v59, vcc
	v_fma_f32 v58, v59, v59, 1.0
	v_rsq_f32_e32 v61, v58
	s_nop 0
	v_mul_f32_e32 v62, v61, v59
	v_mul_f32_e32 v55, v62, v54
	v_mul_f32_e32 v56, v62, v53
	v_fma_f32 v53, v61, v53, -v55
	v_fma_f32 v54, v61, v54, v56
	v_mul_f32_e32 v55, v52, v52
	v_mul_f32_e32 v56, v53, v53
	v_mul_f32_e32 v57, v52, v53
	v_add_f32_dpp v55, v55, v55 quad_perm:[1,0,3,2] row_mask:0xf bank_mask:0xf
	v_add_f32_dpp v56, v56, v56 quad_perm:[1,0,3,2] row_mask:0xf bank_mask:0xf
	v_add_f32_dpp v57, v57, v57 quad_perm:[1,0,3,2] row_mask:0xf bank_mask:0xf
	v_add_f32_dpp v55, v55, v55 quad_perm:[2,3,0,1] row_mask:0xf bank_mask:0xf
	v_add_f32_dpp v56, v56, v56 quad_perm:[2,3,0,1] row_mask:0xf bank_mask:0xf
	v_add_f32_dpp v57, v57, v57 quad_perm:[2,3,0,1] row_mask:0xf bank_mask:0xf
	v_sub_f32_e32 v60, v56, v55
	v_mul_f32_e32 v58, v57, v57
	v_cmp_gt_f32_e32 vcc, 0, v60
	v_mul_f32_e32 v59, v60, v60
	v_fmac_f32_e32 v59, 4.0, v58
	v_sqrt_f32_e32 v59, v59
	v_mul_f32_e32 v63, v62, v42
	v_mul_f32_e32 v43, v62, v41
	v_fma_f32 v41, v61, v41, -v63
	v_fma_f32 v42, v61, v42, v43
	v_add_f32_e64 v59, |v60|, v59
	v_add_f32_e32 v59, 0x0da24260, v59
	v_rcp_f32_e32 v59, v59
	v_add_f32_e32 v58, v57, v57
	v_mul_f32_e32 v59, v58, v59
	v_cndmask_b32_e64 v59, v59, -v59, vcc
	v_fma_f32 v58, v59, v59, 1.0
	v_rsq_f32_e32 v61, v58
	s_nop 0
	v_mul_f32_e32 v62, v61, v59
	v_mul_f32_e32 v55, v62, v53
	v_mul_f32_e32 v56, v62, v52
	v_fma_f32 v52, v61, v52, -v55
	v_fma_f32 v53, v61, v53, v56
	v_mul_f32_e32 v55, v52, v52
	v_mul_f32_e32 v56, v54, v54
	v_mul_f32_e32 v57, v52, v54
	v_add_f32_dpp v55, v55, v55 quad_perm:[1,0,3,2] row_mask:0xf bank_mask:0xf
	v_add_f32_dpp v56, v56, v56 quad_perm:[1,0,3,2] row_mask:0xf bank_mask:0xf
	v_add_f32_dpp v57, v57, v57 quad_perm:[1,0,3,2] row_mask:0xf bank_mask:0xf
	v_add_f32_dpp v55, v55, v55 quad_perm:[2,3,0,1] row_mask:0xf bank_mask:0xf
	v_add_f32_dpp v56, v56, v56 quad_perm:[2,3,0,1] row_mask:0xf bank_mask:0xf
	v_add_f32_dpp v57, v57, v57 quad_perm:[2,3,0,1] row_mask:0xf bank_mask:0xf
	v_sub_f32_e32 v60, v56, v55
	v_mul_f32_e32 v58, v57, v57
	v_cmp_gt_f32_e32 vcc, 0, v60
	v_mul_f32_e32 v59, v60, v60
	v_fmac_f32_e32 v59, 4.0, v58
	v_sqrt_f32_e32 v59, v59
	v_mul_f32_e32 v63, v62, v41
	v_mul_f32_e32 v43, v62, v40
	v_fma_f32 v40, v61, v40, -v63
	v_fma_f32 v41, v61, v41, v43
	v_add_f32_e64 v59, |v60|, v59
	v_add_f32_e32 v59, 0x0da24260, v59
	v_rcp_f32_e32 v59, v59
	v_add_f32_e32 v58, v57, v57
	v_mul_f32_e32 v59, v58, v59
	v_cndmask_b32_e64 v59, v59, -v59, vcc
	v_fma_f32 v58, v59, v59, 1.0
	v_rsq_f32_e32 v61, v58
	s_nop 0
	v_mul_f32_e32 v62, v61, v59
	v_mul_f32_e32 v55, v62, v54
	v_mul_f32_e32 v56, v62, v52
	v_fma_f32 v52, v61, v52, -v55
	v_fma_f32 v54, v61, v54, v56
	v_mul_f32_e32 v55, v53, v53
	v_mul_f32_e32 v56, v54, v54
	v_mul_f32_e32 v57, v53, v54
	v_add_f32_dpp v55, v55, v55 quad_perm:[1,0,3,2] row_mask:0xf bank_mask:0xf
	v_add_f32_dpp v56, v56, v56 quad_perm:[1,0,3,2] row_mask:0xf bank_mask:0xf
	v_add_f32_dpp v57, v57, v57 quad_perm:[1,0,3,2] row_mask:0xf bank_mask:0xf
	v_add_f32_dpp v55, v55, v55 quad_perm:[2,3,0,1] row_mask:0xf bank_mask:0xf
	v_add_f32_dpp v56, v56, v56 quad_perm:[2,3,0,1] row_mask:0xf bank_mask:0xf
	v_add_f32_dpp v57, v57, v57 quad_perm:[2,3,0,1] row_mask:0xf bank_mask:0xf
	v_sub_f32_e32 v60, v56, v55
	v_mul_f32_e32 v58, v57, v57
	v_cmp_gt_f32_e32 vcc, 0, v60
	v_mul_f32_e32 v59, v60, v60
	v_fmac_f32_e32 v59, 4.0, v58
	v_sqrt_f32_e32 v59, v59
	v_mul_f32_e32 v63, v62, v42
	v_mul_f32_e32 v43, v62, v40
	v_fma_f32 v40, v61, v40, -v63
	v_fma_f32 v42, v61, v42, v43
	v_add_f32_e64 v59, |v60|, v59
	v_add_f32_e32 v59, 0x0da24260, v59
	v_rcp_f32_e32 v59, v59
	v_add_f32_e32 v58, v57, v57
	v_mul_f32_e32 v59, v58, v59
	v_cndmask_b32_e64 v59, v59, -v59, vcc
	v_fma_f32 v58, v59, v59, 1.0
	v_rsq_f32_e32 v61, v58
	s_nop 0
	v_mul_f32_e32 v62, v61, v59
	v_mul_f32_e32 v55, v62, v54
	v_mul_f32_e32 v56, v62, v53
	v_fma_f32 v53, v61, v53, -v55
	v_fma_f32 v54, v61, v54, v56
	v_mul_f32_e32 v55, v52, v52
	v_mul_f32_e32 v56, v53, v53
	v_mul_f32_e32 v57, v52, v53
	v_add_f32_dpp v55, v55, v55 quad_perm:[1,0,3,2] row_mask:0xf bank_mask:0xf
	v_add_f32_dpp v56, v56, v56 quad_perm:[1,0,3,2] row_mask:0xf bank_mask:0xf
	v_add_f32_dpp v57, v57, v57 quad_perm:[1,0,3,2] row_mask:0xf bank_mask:0xf
	v_add_f32_dpp v55, v55, v55 quad_perm:[2,3,0,1] row_mask:0xf bank_mask:0xf
	v_add_f32_dpp v56, v56, v56 quad_perm:[2,3,0,1] row_mask:0xf bank_mask:0xf
	v_add_f32_dpp v57, v57, v57 quad_perm:[2,3,0,1] row_mask:0xf bank_mask:0xf
	v_sub_f32_e32 v60, v56, v55
	v_mul_f32_e32 v58, v57, v57
	v_cmp_gt_f32_e32 vcc, 0, v60
	v_mul_f32_e32 v59, v60, v60
	v_fmac_f32_e32 v59, 4.0, v58
	v_sqrt_f32_e32 v59, v59
	v_mul_f32_e32 v63, v62, v42
	v_mul_f32_e32 v43, v62, v41
	v_fma_f32 v41, v61, v41, -v63
	v_fma_f32 v42, v61, v42, v43
	v_add_f32_e64 v59, |v60|, v59
	v_add_f32_e32 v59, 0x0da24260, v59
	v_rcp_f32_e32 v59, v59
	v_add_f32_e32 v58, v57, v57
	v_mul_f32_e32 v59, v58, v59
	v_cndmask_b32_e64 v59, v59, -v59, vcc
	v_fma_f32 v58, v59, v59, 1.0
	v_rsq_f32_e32 v61, v58
	s_nop 0
	v_mul_f32_e32 v62, v61, v59
	v_mul_f32_e32 v55, v62, v53
	v_mul_f32_e32 v56, v62, v52
	v_fma_f32 v52, v61, v52, -v55
	v_fma_f32 v53, v61, v53, v56
	v_mul_f32_e32 v55, v52, v52
	v_mul_f32_e32 v56, v54, v54
	v_mul_f32_e32 v57, v52, v54
	v_add_f32_dpp v55, v55, v55 quad_perm:[1,0,3,2] row_mask:0xf bank_mask:0xf
	v_add_f32_dpp v56, v56, v56 quad_perm:[1,0,3,2] row_mask:0xf bank_mask:0xf
	v_add_f32_dpp v57, v57, v57 quad_perm:[1,0,3,2] row_mask:0xf bank_mask:0xf
	v_add_f32_dpp v55, v55, v55 quad_perm:[2,3,0,1] row_mask:0xf bank_mask:0xf
	v_add_f32_dpp v56, v56, v56 quad_perm:[2,3,0,1] row_mask:0xf bank_mask:0xf
	v_add_f32_dpp v57, v57, v57 quad_perm:[2,3,0,1] row_mask:0xf bank_mask:0xf
	v_sub_f32_e32 v60, v56, v55
	v_mul_f32_e32 v58, v57, v57
	v_cmp_gt_f32_e32 vcc, 0, v60
	v_mul_f32_e32 v59, v60, v60
	v_fmac_f32_e32 v59, 4.0, v58
	v_sqrt_f32_e32 v59, v59
	v_mul_f32_e32 v63, v62, v41
	v_mul_f32_e32 v43, v62, v40
	v_fma_f32 v40, v61, v40, -v63
	v_fma_f32 v41, v61, v41, v43
	v_add_f32_e64 v59, |v60|, v59
	v_add_f32_e32 v59, 0x0da24260, v59
	v_rcp_f32_e32 v59, v59
	v_add_f32_e32 v58, v57, v57
	v_mul_f32_e32 v59, v58, v59
	v_cndmask_b32_e64 v59, v59, -v59, vcc
	v_fma_f32 v58, v59, v59, 1.0
	v_rsq_f32_e32 v61, v58
	s_nop 0
	v_mul_f32_e32 v62, v61, v59
	v_mul_f32_e32 v55, v62, v54
	v_mul_f32_e32 v56, v62, v52
	v_fma_f32 v52, v61, v52, -v55
	v_fma_f32 v54, v61, v54, v56
	v_mul_f32_e32 v55, v53, v53
	v_mul_f32_e32 v56, v54, v54
	v_mul_f32_e32 v57, v53, v54
	v_add_f32_dpp v55, v55, v55 quad_perm:[1,0,3,2] row_mask:0xf bank_mask:0xf
	v_add_f32_dpp v56, v56, v56 quad_perm:[1,0,3,2] row_mask:0xf bank_mask:0xf
	v_add_f32_dpp v57, v57, v57 quad_perm:[1,0,3,2] row_mask:0xf bank_mask:0xf
	v_add_f32_dpp v55, v55, v55 quad_perm:[2,3,0,1] row_mask:0xf bank_mask:0xf
	v_add_f32_dpp v56, v56, v56 quad_perm:[2,3,0,1] row_mask:0xf bank_mask:0xf
	v_add_f32_dpp v57, v57, v57 quad_perm:[2,3,0,1] row_mask:0xf bank_mask:0xf
	v_sub_f32_e32 v60, v56, v55
	v_mul_f32_e32 v58, v57, v57
	v_cmp_gt_f32_e32 vcc, 0, v60
	v_mul_f32_e32 v59, v60, v60
	v_fmac_f32_e32 v59, 4.0, v58
	v_sqrt_f32_e32 v59, v59
	v_mul_f32_e32 v63, v62, v42
	v_mul_f32_e32 v43, v62, v40
	v_fma_f32 v40, v61, v40, -v63
	v_fma_f32 v42, v61, v42, v43
	v_add_f32_e64 v59, |v60|, v59
	v_add_f32_e32 v59, 0x0da24260, v59
	v_rcp_f32_e32 v59, v59
	v_add_f32_e32 v58, v57, v57
	v_mul_f32_e32 v59, v58, v59
	v_cndmask_b32_e64 v59, v59, -v59, vcc
	v_fma_f32 v58, v59, v59, 1.0
	v_rsq_f32_e32 v61, v58
	s_nop 0
	v_mul_f32_e32 v62, v61, v59
	v_mul_f32_e32 v55, v62, v54
	v_mul_f32_e32 v56, v62, v53
	v_fma_f32 v53, v61, v53, -v55
	v_fma_f32 v54, v61, v54, v56
	v_mul_f32_e32 v63, v62, v42
	v_mul_f32_e32 v43, v62, v41
	v_fma_f32 v41, v61, v41, -v63
	v_fma_f32 v42, v61, v42, v43
	v_mul_f32_e32 v55, v52, v52
	v_mul_f32_e32 v56, v53, v53
	v_mul_f32_e32 v57, v54, v54
	v_add_f32_dpp v55, v55, v55 quad_perm:[1,0,3,2] row_mask:0xf bank_mask:0xf
	v_add_f32_dpp v56, v56, v56 quad_perm:[1,0,3,2] row_mask:0xf bank_mask:0xf
	v_add_f32_dpp v57, v57, v57 quad_perm:[1,0,3,2] row_mask:0xf bank_mask:0xf
	v_add_f32_dpp v55, v55, v55 quad_perm:[2,3,0,1] row_mask:0xf bank_mask:0xf
	v_add_f32_dpp v56, v56, v56 quad_perm:[2,3,0,1] row_mask:0xf bank_mask:0xf
	v_add_f32_dpp v57, v57, v57 quad_perm:[2,3,0,1] row_mask:0xf bank_mask:0xf
	v_cmp_le_f32_e64 s[28:29], v55, v56
	v_cmp_le_f32_e64 s[30:31], v55, v57
	v_cmp_lt_f32_e32 vcc, v57, v56
	s_and_b64 s[28:29], s[28:29], s[30:31]
	s_andn2_b64 s[30:31], vcc, s[28:29]
	v_cndmask_b32_e64 v44, v52, v53, s[28:29]
	v_cndmask_b32_e64 v45, v54, v53, s[30:31]
	v_cndmask_b32_e64 v46, v40, v41, s[28:29]
	v_cndmask_b32_e64 v47, v42, v41, s[30:31]
	v_mul_f32_e32 v58, v44, v44
	s_nop 1
	v_add_f32_dpp v58, v58, v58 quad_perm:[1,0,3,2] row_mask:0xf bank_mask:0xf
	s_nop 1
	v_add_f32_dpp v58, v58, v58 quad_perm:[2,3,0,1] row_mask:0xf bank_mask:0xf
	v_max_f32_e32 v58, 0x3aa2425, v58
	v_rsq_f32_e32 v58, v58
	s_nop 0
	v_mul_f32_e32 v48, v44, v58
	v_mul_f32_e32 v59, v48, v45
	s_nop 1
	v_add_f32_dpp v59, v59, v59 quad_perm:[1,0,3,2] row_mask:0xf bank_mask:0xf
	s_nop 1
	v_add_f32_dpp v59, v59, v59 quad_perm:[2,3,0,1] row_mask:0xf bank_mask:0xf
	v_fma_f32 v49, -v59, v48, v45
	v_mul_f32_e32 v58, v49, v49
	s_nop 1
	v_add_f32_dpp v58, v58, v58 quad_perm:[1,0,3,2] row_mask:0xf bank_mask:0xf
	s_nop 1
	v_add_f32_dpp v58, v58, v58 quad_perm:[2,3,0,1] row_mask:0xf bank_mask:0xf
	v_max_f32_e32 v58, 0x3aa2425, v58
	v_rsq_f32_e32 v58, v58
	s_nop 0
	v_mul_f32_e32 v50, v49, v58
	v_mov_b32_dpp v43, v47 quad_perm:[2,0,1,3] row_mask:0xf bank_mask:0xf
	v_mov_b32_dpp v63, v47 quad_perm:[1,2,0,3] row_mask:0xf bank_mask:0xf
	v_mov_b32_dpp v62, v50 quad_perm:[2,0,1,3] row_mask:0xf bank_mask:0xf
	v_mov_b32_dpp v61, v50 quad_perm:[1,2,0,3] row_mask:0xf bank_mask:0xf
	v_mul_f32_dpp v60, v46, v43 quad_perm:[1,2,0,3] row_mask:0xf bank_mask:0xf
	v_mul_f32_dpp v51, v48, v62 quad_perm:[1,2,0,3] row_mask:0xf bank_mask:0xf
	s_nop 0
	v_fmac_f32_dpp v60, -v46, v63 quad_perm:[2,0,1,3] row_mask:0xf bank_mask:0xf
	v_fmac_f32_dpp v51, -v48, v61 quad_perm:[2,0,1,3] row_mask:0xf bank_mask:0xf
	v_mul_f32_dpp v52, v46, v48 quad_perm:[0,0,0,0] row_mask:0xf bank_mask:0xf
	v_mul_f32_dpp v53, v46, v48 quad_perm:[1,1,1,1] row_mask:0xf bank_mask:0xf
	v_mul_f32_dpp v54, v46, v48 quad_perm:[2,2,2,2] row_mask:0xf bank_mask:0xf
	v_fmac_f32_dpp v52, v47, v50 quad_perm:[0,0,0,0] row_mask:0xf bank_mask:0xf
	v_fmac_f32_dpp v53, v47, v50 quad_perm:[1,1,1,1] row_mask:0xf bank_mask:0xf
	v_fmac_f32_dpp v54, v47, v50 quad_perm:[2,2,2,2] row_mask:0xf bank_mask:0xf
	v_fmac_f32_dpp v52, v60, v51 quad_perm:[0,0,0,0] row_mask:0xf bank_mask:0xf
	v_fmac_f32_dpp v53, v60, v51 quad_perm:[1,1,1,1] row_mask:0xf bank_mask:0xf
	v_fmac_f32_dpp v54, v60, v51 quad_perm:[2,2,2,2] row_mask:0xf bank_mask:0xf
	v_mov_b32_e32 v55, 0
	v_writelane_b32 v55, s32, 48
	v_writelane_b32 v55, s33, 49
	v_writelane_b32 v55, s34, 50
	v_mul_f32_e32 v55, 0xbc800000, v55
	v_mul_f32_e32 v56, v55, v52
	v_mul_f32_e32 v57, v55, v53
	v_mul_f32_e32 v58, v55, v54
	v_add_f32_dpp v56, v56, v56 quad_perm:[1,0,3,2] row_mask:0xf bank_mask:0xf
	v_add_f32_dpp v57, v57, v57 quad_perm:[1,0,3,2] row_mask:0xf bank_mask:0xf
	v_add_f32_dpp v58, v58, v58 quad_perm:[1,0,3,2] row_mask:0xf bank_mask:0xf
	v_add_f32_dpp v56, v56, v56 quad_perm:[2,3,0,1] row_mask:0xf bank_mask:0xf
	v_add_f32_dpp v57, v57, v57 quad_perm:[2,3,0,1] row_mask:0xf bank_mask:0xf
	v_add_f32_dpp v58, v58, v58 quad_perm:[2,3,0,1] row_mask:0xf bank_mask:0xf
	v_cndmask_b32_e64 v52, v52, v56, s[26:27]
	v_cndmask_b32_e64 v53, v53, v57, s[26:27]
	v_cndmask_b32_e64 v54, v54, v58, s[26:27]
	v_subrev_u32_e32 v59, 48, v0
	v_lshlrev_b32_e32 v59, 4, v59
	s_mov_b32 s20, 0
	s_mov_b32 s21, 0xf0000
	s_mov_b64 exec, s[20:21]
	ds_write_b96 v59, v[52:54] offset:12288
	s_mov_b64 exec, -1
	s_branch .Ljoin

.Ljoin:
	s_waitcnt vmcnt(3)
	ds_write_b128 v2, v[8:11]
	ds_write_b128 v2, v[12:15] offset:1024
	ds_write_b128 v2, v[16:19] offset:2048
	s_waitcnt lgkmcnt(0)
	s_barrier
	v_mov_b32_e32 v6, 0x3000
	ds_read_b96 v[32:34], v6
	ds_read_b96 v[36:38], v6 offset:16
	ds_read_b96 v[40:42], v6 offset:32
	ds_read_b96 v[44:46], v6 offset:48
	ds_read2_b32 v[48:49], v3 offset0:0 offset1:1
	ds_read_b32 v56, v3 offset:8
	ds_read2_b32 v[50:51], v3 offset0:192 offset1:193
	ds_read_b32 v57, v3 offset:776
	ds_read2_b32 v[52:53], v4 offset0:0 offset1:1
	ds_read_b32 v58, v4 offset:8
	ds_read2_b32 v[54:55], v4 offset0:192 offset1:193
	ds_read_b32 v59, v4 offset:776
	s_waitcnt lgkmcnt(6)
	v_fma_f32 v60, v48, v32, v44
	v_fma_f32 v61, v48, v33, v45
	v_fma_f32 v62, v48, v34, v46
	v_fmac_f32_e32 v60, v49, v36
	v_fmac_f32_e32 v61, v49, v37
	v_fmac_f32_e32 v62, v49, v38
	v_fmac_f32_e32 v60, v56, v40
	v_fmac_f32_e32 v61, v56, v41
	v_fmac_f32_e32 v62, v56, v42
	ds_write2_b32 v3, v60, v61 offset0:0 offset1:1
	ds_write_b32 v3, v62 offset:8
	s_waitcnt lgkmcnt(6)
	v_fma_f32 v35, v50, v32, v44
	v_fma_f32 v39, v50, v33, v45
	v_fma_f32 v43, v50, v34, v46
	v_fmac_f32_e32 v35, v51, v36
	v_fmac_f32_e32 v39, v51, v37
	v_fmac_f32_e32 v43, v51, v38
	v_fmac_f32_e32 v35, v57, v40
	v_fmac_f32_e32 v39, v57, v41
	v_fmac_f32_e32 v43, v57, v42
	ds_write2_b32 v3, v35, v39 offset0:192 offset1:193
	ds_write_b32 v3, v43 offset:776
	s_waitcnt lgkmcnt(6)
	v_fma_f32 v60, v52, v32, v44
	v_fma_f32 v61, v52, v33, v45
	v_fma_f32 v62, v52, v34, v46
	v_fmac_f32_e32 v60, v53, v36
	v_fmac_f32_e32 v61, v53, v37
	v_fmac_f32_e32 v62, v53, v38
	v_fmac_f32_e32 v60, v58, v40
	v_fmac_f32_e32 v61, v58, v41
	v_fmac_f32_e32 v62, v58, v42
	ds_write2_b32 v4, v60, v61 offset0:0 offset1:1
	ds_write_b32 v4, v62 offset:8
	s_waitcnt lgkmcnt(6)
	v_fma_f32 v35, v54, v32, v44
	v_fma_f32 v39, v54, v33, v45
	v_fma_f32 v43, v54, v34, v46
	v_fmac_f32_e32 v35, v55, v36
	v_fmac_f32_e32 v39, v55, v37
	v_fmac_f32_e32 v43, v55, v38
	v_fmac_f32_e32 v35, v59, v40
	v_fmac_f32_e32 v39, v59, v41
	v_fmac_f32_e32 v43, v59, v42
	ds_write2_b32 v4, v35, v39 offset0:192 offset1:193
	ds_write_b32 v4, v43 offset:776
	ds_read_b128 v[8:11], v2
	ds_read_b128 v[12:15], v2 offset:1024
	ds_read_b128 v[16:19], v2 offset:2048
	s_waitcnt lgkmcnt(2)
	global_store_dwordx4 v1, v[8:11], s[10:11] offset:-2048 sc1 nt
	s_waitcnt lgkmcnt(1)
	global_store_dwordx4 v1, v[12:15], s[10:11] offset:-1024 sc1 nt
	s_waitcnt lgkmcnt(0)
	global_store_dwordx4 v1, v[16:19], s[10:11] offset:0 sc1 nt
	s_waitcnt vmcnt(3)
	ds_write_b128 v2, v[20:23]
	ds_write_b128 v2, v[24:27] offset:1024
	ds_write_b128 v2, v[28:31] offset:2048
	ds_read2_b32 v[48:49], v3 offset0:0 offset1:1
	ds_read_b32 v56, v3 offset:8
	ds_read2_b32 v[50:51], v3 offset0:192 offset1:193
	ds_read_b32 v57, v3 offset:776
	ds_read2_b32 v[52:53], v4 offset0:0 offset1:1
	ds_read_b32 v58, v4 offset:8
	ds_read2_b32 v[54:55], v4 offset0:192 offset1:193
	ds_read_b32 v59, v4 offset:776
	s_waitcnt lgkmcnt(6)
	v_fma_f32 v60, v48, v32, v44
	v_fma_f32 v61, v48, v33, v45
	v_fma_f32 v62, v48, v34, v46
	v_fmac_f32_e32 v60, v49, v36
	v_fmac_f32_e32 v61, v49, v37
	v_fmac_f32_e32 v62, v49, v38
	v_fmac_f32_e32 v60, v56, v40
	v_fmac_f32_e32 v61, v56, v41
	v_fmac_f32_e32 v62, v56, v42
	ds_write2_b32 v3, v60, v61 offset0:0 offset1:1
	ds_write_b32 v3, v62 offset:8
	s_waitcnt lgkmcnt(6)
	v_fma_f32 v35, v50, v32, v44
	v_fma_f32 v39, v50, v33, v45
	v_fma_f32 v43, v50, v34, v46
	v_fmac_f32_e32 v35, v51, v36
	v_fmac_f32_e32 v39, v51, v37
	v_fmac_f32_e32 v43, v51, v38
	v_fmac_f32_e32 v35, v57, v40
	v_fmac_f32_e32 v39, v57, v41
	v_fmac_f32_e32 v43, v57, v42
	ds_write2_b32 v3, v35, v39 offset0:192 offset1:193
	ds_write_b32 v3, v43 offset:776
	s_waitcnt lgkmcnt(6)
	v_fma_f32 v60, v52, v32, v44
	v_fma_f32 v61, v52, v33, v45
	v_fma_f32 v62, v52, v34, v46
	v_fmac_f32_e32 v60, v53, v36
	v_fmac_f32_e32 v61, v53, v37
	v_fmac_f32_e32 v62, v53, v38
	v_fmac_f32_e32 v60, v58, v40
	v_fmac_f32_e32 v61, v58, v41
	v_fmac_f32_e32 v62, v58, v42
	ds_write2_b32 v4, v60, v61 offset0:0 offset1:1
	ds_write_b32 v4, v62 offset:8
	s_waitcnt lgkmcnt(6)
	v_fma_f32 v35, v54, v32, v44
	v_fma_f32 v39, v54, v33, v45
	v_fma_f32 v43, v54, v34, v46
	v_fmac_f32_e32 v35, v55, v36
	v_fmac_f32_e32 v39, v55, v37
	v_fmac_f32_e32 v43, v55, v38
	v_fmac_f32_e32 v35, v59, v40
	v_fmac_f32_e32 v39, v59, v41
	v_fmac_f32_e32 v43, v59, v42
	ds_write2_b32 v4, v35, v39 offset0:192 offset1:193
	ds_write_b32 v4, v43 offset:776
	ds_read_b128 v[20:23], v2
	ds_read_b128 v[24:27], v2 offset:1024
	ds_read_b128 v[28:31], v2 offset:2048
	s_waitcnt lgkmcnt(2)
	global_store_dwordx4 v1, v[20:23], s[10:11] offset:1024 sc1 nt
	s_waitcnt lgkmcnt(1)
	global_store_dwordx4 v1, v[24:27], s[10:11] offset:2048 sc1 nt
	s_waitcnt lgkmcnt(0)
	s_and_saveexec_b64 s[16:17], s[14:15]
	global_store_dwordx4 v1, v[28:31], s[10:11] offset:3072 sc1 nt
	s_endpgm
